# P1 K-loop: all remaining LDS-DMA pieces to scalar-base form (odd-step row base kept in s[98:99], vcc as scratch base pair), 10 64-bit VALU adds per iteration replaced by 4 SALU
# baseline (speedup 1.0000x reference)
.Lp1_first:
	ds_read_b128 v[184:187], v175
	ds_read_b128 v[188:191], v176
	ds_read_b128 v[192:195], v175 offset:2048
	ds_read_b128 v[196:199], v176 offset:2048
	ds_read_b128 v[200:203], v175 offset:16384
	ds_read_b128 v[204:207], v176 offset:16384
	ds_read_b128 v[208:211], v175 offset:18432
	ds_read_b128 v[212:215], v176 offset:18432
	s_add_u32 vcc_lo, s98, s66
	s_addc_u32 vcc_hi, s99, s67
	s_add_i32 m0, s77, 0x8000
	ds_read_b128 v[216:219], v178
	ds_read_b128 v[220:223], v178 offset:2048
	ds_read_b128 v[224:227], v179
	ds_read_b128 v[228:231], v179 offset:2048
	ds_read_b128 v[232:235], v178 offset:4096
	ds_read_b128 v[236:239], v178 offset:6144
	ds_read_b128 v[240:243], v179 offset:4096
	ds_read_b128 v[244:247], v179 offset:6144
	global_load_lds_dwordx4 v146, vcc
	s_add_i32 m0, s77, 0xa000
	s_nop 0
	global_load_lds_dwordx4 v130, vcc
	s_add_i32 m0, s77, 0xc000
	s_nop 0
	global_load_lds_dwordx4 v132, vcc
	s_add_i32 m0, s77, 0xe000
	s_nop 0
	global_load_lds_dwordx4 v134, vcc
	s_waitcnt vmcnt(8)
	s_waitcnt lgkmcnt(0)
	s_barrier
	s_setprio 1
	s_waitcnt lgkmcnt(0)
	v_mfma_f32_16x16x32_bf16 v[126:129], v[184:187], v[216:219], 0
	s_add_u32 s70, s64, s66
	s_addc_u32 s71, s65, s67
	s_add_u32 s73, s70, 0x100
	s_addc_u32 vcc_lo, s71, 0
	v_mfma_f32_16x16x32_bf16 v[122:125], v[192:195], v[216:219], 0
	s_and_b64 s[70:71], s[68:69], exec
	s_cselect_b32 s71, s47, vcc_lo
	s_cselect_b32 s70, s46, s73
	s_add_u32 s73, s15, s66
	v_mfma_f32_16x16x32_bf16 v[118:121], v[184:187], v[220:223], 0
	s_addc_u32 vcc_lo, s43, s67
	s_and_b64 s[68:69], s[68:69], exec
	s_cselect_b32 s69, s45, vcc_lo
	s_cselect_b32 s68, s44, s73
	v_mfma_f32_16x16x32_bf16 v[114:117], v[192:195], v[220:223], 0
	v_mfma_f32_16x16x32_bf16 v[110:113], v[184:187], v[232:235], 0
	v_mfma_f32_16x16x32_bf16 v[106:109], v[192:195], v[232:235], 0
	v_mfma_f32_16x16x32_bf16 v[102:105], v[184:187], v[236:239], 0
	v_mfma_f32_16x16x32_bf16 v[98:101], v[192:195], v[236:239], 0
	v_mfma_f32_16x16x32_bf16 v[126:129], v[188:191], v[224:227], v[126:129]
	v_mfma_f32_16x16x32_bf16 v[122:125], v[196:199], v[224:227], v[122:125]
	v_mfma_f32_16x16x32_bf16 v[118:121], v[188:191], v[228:231], v[118:121]
	v_mfma_f32_16x16x32_bf16 v[114:117], v[196:199], v[228:231], v[114:117]
	v_mfma_f32_16x16x32_bf16 v[110:113], v[188:191], v[240:243], v[110:113]
	v_mfma_f32_16x16x32_bf16 v[106:109], v[196:199], v[240:243], v[106:109]
	v_mfma_f32_16x16x32_bf16 v[102:105], v[188:191], v[244:247], v[102:105]
	v_mfma_f32_16x16x32_bf16 v[98:101], v[196:199], v[244:247], v[98:101]
	s_setprio 0
	s_setprio 1
	v_mfma_f32_16x16x32_bf16 v[62:65], v[200:203], v[216:219], 0
	v_mfma_f32_16x16x32_bf16 v[58:61], v[208:211], v[216:219], 0
	v_mfma_f32_16x16x32_bf16 v[54:57], v[200:203], v[220:223], 0
	v_mfma_f32_16x16x32_bf16 v[50:53], v[208:211], v[220:223], 0
	v_mfma_f32_16x16x32_bf16 v[46:49], v[200:203], v[232:235], 0
	v_mfma_f32_16x16x32_bf16 v[42:45], v[208:211], v[232:235], 0
	v_mfma_f32_16x16x32_bf16 v[38:41], v[200:203], v[236:239], 0
	v_mfma_f32_16x16x32_bf16 v[34:37], v[208:211], v[236:239], 0
	v_mfma_f32_16x16x32_bf16 v[62:65], v[204:207], v[224:227], v[62:65]
	v_mfma_f32_16x16x32_bf16 v[58:61], v[212:215], v[224:227], v[58:61]
	v_mfma_f32_16x16x32_bf16 v[54:57], v[204:207], v[228:231], v[54:57]
	v_mfma_f32_16x16x32_bf16 v[50:53], v[212:215], v[228:231], v[50:53]
	v_mfma_f32_16x16x32_bf16 v[46:49], v[204:207], v[240:243], v[46:49]
	v_mfma_f32_16x16x32_bf16 v[42:45], v[212:215], v[240:243], v[42:45]
	v_mfma_f32_16x16x32_bf16 v[38:41], v[204:207], v[244:247], v[38:41]
	v_mfma_f32_16x16x32_bf16 v[34:37], v[212:215], v[244:247], v[34:37]
	s_setprio 0
	s_barrier
	s_add_i32 s73, s87, s76
	s_mov_b32 m0, s73
	ds_read_b128 v[216:219], v178 offset:16384
	ds_read_b128 v[220:223], v178 offset:18432
	ds_read_b128 v[224:227], v179 offset:16384
	ds_read_b128 v[228:231], v179 offset:18432
	ds_read_b128 v[232:235], v178 offset:20480
	ds_read_b128 v[236:239], v178 offset:22528
	ds_read_b128 v[240:243], v179 offset:20480
	ds_read_b128 v[244:247], v179 offset:22528
	global_load_lds_dwordx4 v142, s[68:69]
	s_add_i32 m0, s73, 0x2000
	s_add_u32 vcc_lo, s68, 0x80000
	s_addc_u32 vcc_hi, s69, 0
	s_add_i32 s73, s89, s76
	global_load_lds_dwordx4 v144, s[68:69]
	s_mov_b32 m0, s73
	s_nop 0
	global_load_lds_dwordx4 v142, vcc
	s_add_i32 m0, s73, 0x2000
	s_nop 0
	global_load_lds_dwordx4 v144, vcc
	s_waitcnt vmcnt(6)
	s_waitcnt lgkmcnt(0)
	s_barrier
	s_setprio 1
	s_waitcnt lgkmcnt(0)
	v_mfma_f32_16x16x32_bf16 v[94:97], v[184:187], v[216:219], 0
	v_mfma_f32_16x16x32_bf16 v[90:93], v[192:195], v[216:219], 0
	v_mfma_f32_16x16x32_bf16 v[86:89], v[184:187], v[220:223], 0
	v_mfma_f32_16x16x32_bf16 v[82:85], v[192:195], v[220:223], 0
	v_mfma_f32_16x16x32_bf16 v[78:81], v[184:187], v[232:235], 0
	v_mfma_f32_16x16x32_bf16 v[74:77], v[192:195], v[232:235], 0
	v_mfma_f32_16x16x32_bf16 v[70:73], v[184:187], v[236:239], 0
	v_mfma_f32_16x16x32_bf16 v[66:69], v[192:195], v[236:239], 0
	v_mfma_f32_16x16x32_bf16 v[94:97], v[188:191], v[224:227], v[94:97]
	v_mfma_f32_16x16x32_bf16 v[90:93], v[196:199], v[224:227], v[90:93]
	v_mfma_f32_16x16x32_bf16 v[86:89], v[188:191], v[228:231], v[86:89]
	v_mfma_f32_16x16x32_bf16 v[82:85], v[196:199], v[228:231], v[82:85]
	v_mfma_f32_16x16x32_bf16 v[78:81], v[188:191], v[240:243], v[78:81]
	v_mfma_f32_16x16x32_bf16 v[74:77], v[196:199], v[240:243], v[74:77]
	v_mfma_f32_16x16x32_bf16 v[70:73], v[188:191], v[244:247], v[70:73]
	v_mfma_f32_16x16x32_bf16 v[66:69], v[196:199], v[244:247], v[66:69]
	s_setprio 0
	s_setprio 1
	v_mfma_f32_16x16x32_bf16 v[30:33], v[200:203], v[216:219], 0
	v_mfma_f32_16x16x32_bf16 v[26:29], v[208:211], v[216:219], 0
	v_mfma_f32_16x16x32_bf16 v[22:25], v[200:203], v[220:223], 0
	v_mfma_f32_16x16x32_bf16 v[18:21], v[208:211], v[220:223], 0
	v_mfma_f32_16x16x32_bf16 v[14:17], v[200:203], v[232:235], 0
	v_mfma_f32_16x16x32_bf16 v[10:13], v[208:211], v[232:235], 0
	v_mfma_f32_16x16x32_bf16 v[6:9], v[200:203], v[236:239], 0
	v_mfma_f32_16x16x32_bf16 v[2:5], v[208:211], v[236:239], 0
	v_mfma_f32_16x16x32_bf16 v[30:33], v[204:207], v[224:227], v[30:33]
	v_mfma_f32_16x16x32_bf16 v[26:29], v[212:215], v[224:227], v[26:29]
	v_mfma_f32_16x16x32_bf16 v[22:25], v[204:207], v[228:231], v[22:25]
	v_mfma_f32_16x16x32_bf16 v[18:21], v[212:215], v[228:231], v[18:21]
	v_mfma_f32_16x16x32_bf16 v[14:17], v[204:207], v[240:243], v[14:17]
	v_mfma_f32_16x16x32_bf16 v[10:13], v[212:215], v[240:243], v[10:13]
	v_mfma_f32_16x16x32_bf16 v[6:9], v[204:207], v[244:247], v[6:9]
	v_mfma_f32_16x16x32_bf16 v[2:5], v[212:215], v[244:247], v[2:5]
	s_setprio 0
	s_barrier
	s_branch .Lp1_blk3

.LBB0_100:
	s_lshl_b32 s15, s14, 19
	s_lshl_b32 s43, s14, 8
	v_or_b32_e32 v2, s15, v172
	s_bitset1_b32 s43, 7
	v_lshlrev_b32_e32 v136, 1, v2
	v_or_b32_e32 v2, s43, v168
	v_lshl_or_b32 v138, v2, 12, v169
	v_or_b32_e32 v2, s15, v173
	s_add_u32 s68, s64, 0x80
	v_lshlrev_b32_e32 v140, 1, v2
	v_or_b32_e32 v2, s43, v170
	s_addc_u32 s69, s65, 0
	v_lshl_or_b32 v150, v2, 12, v171
	v_mov_b32_e32 v131, v147
	v_mov_b32_e32 v133, v147
	v_mov_b32_e32 v135, v147
	s_add_u32 s15, s66, 0x100
	v_mov_b32_e32 v2, 0
	v_mov_b32_e32 v137, v147
	v_mov_b32_e32 v141, v147
	v_mov_b32_e32 v139, v147
	v_mov_b32_e32 v151, v147
	v_lshl_add_u64 v[152:153], s[68:69], 0, v[134:135]
	v_lshl_add_u64 v[154:155], s[68:69], 0, v[132:133]
	v_lshl_add_u64 v[156:157], s[68:69], 0, v[130:131]
	v_lshl_add_u64 v[158:159], s[68:69], 0, v[146:147]
	s_addc_u32 s43, s67, 0
	s_mov_b32 s72, -2
	s_mov_b64 s[66:67], 0
	s_mov_b64 s[98:99], s[68:69]

.LBB0_101:
	s_cmp_eq_u32 s66, 0
	s_cbranch_scc1 .Lp1_first
	ds_read_b128 v[184:187], v175
	ds_read_b128 v[188:191], v176
	ds_read_b128 v[192:195], v175 offset:2048
	ds_read_b128 v[196:199], v176 offset:2048
	ds_read_b128 v[200:203], v175 offset:16384
	ds_read_b128 v[204:207], v176 offset:16384
	ds_read_b128 v[208:211], v175 offset:18432
	ds_read_b128 v[212:215], v176 offset:18432
	s_add_u32 vcc_lo, s98, s66
	s_addc_u32 vcc_hi, s99, s67
	s_add_i32 m0, s77, 0x8000
	ds_read_b128 v[216:219], v178
	ds_read_b128 v[220:223], v178 offset:2048
	ds_read_b128 v[224:227], v179
	ds_read_b128 v[228:231], v179 offset:2048
	ds_read_b128 v[232:235], v178 offset:4096
	ds_read_b128 v[236:239], v178 offset:6144
	ds_read_b128 v[240:243], v179 offset:4096
	ds_read_b128 v[244:247], v179 offset:6144
	global_load_lds_dwordx4 v146, vcc
	s_add_i32 m0, s77, 0xa000
	s_nop 0
	global_load_lds_dwordx4 v130, vcc
	s_add_i32 m0, s77, 0xc000
	s_nop 0
	global_load_lds_dwordx4 v132, vcc
	s_add_i32 m0, s77, 0xe000
	s_nop 0
	global_load_lds_dwordx4 v134, vcc
	s_waitcnt vmcnt(8)
	s_waitcnt lgkmcnt(0)
	s_barrier
	s_setprio 1
	s_waitcnt lgkmcnt(0)
	v_mfma_f32_16x16x32_bf16 v[126:129], v[184:187], v[216:219], v[126:129]
	s_add_u32 s70, s64, s66
	s_addc_u32 s71, s65, s67
	s_add_u32 s73, s70, 0x100
	s_addc_u32 vcc_lo, s71, 0
	v_mfma_f32_16x16x32_bf16 v[122:125], v[192:195], v[216:219], v[122:125]
	s_and_b64 s[70:71], s[68:69], exec
	s_cselect_b32 s71, s47, vcc_lo
	s_cselect_b32 s70, s46, s73
	s_add_u32 s73, s15, s66
	v_mfma_f32_16x16x32_bf16 v[118:121], v[184:187], v[220:223], v[118:121]
	s_addc_u32 vcc_lo, s43, s67
	s_and_b64 s[68:69], s[68:69], exec
	s_cselect_b32 s69, s45, vcc_lo
	s_cselect_b32 s68, s44, s73
	v_mfma_f32_16x16x32_bf16 v[114:117], v[192:195], v[220:223], v[114:117]
	v_mfma_f32_16x16x32_bf16 v[110:113], v[184:187], v[232:235], v[110:113]
	v_mfma_f32_16x16x32_bf16 v[106:109], v[192:195], v[232:235], v[106:109]
	v_mfma_f32_16x16x32_bf16 v[102:105], v[184:187], v[236:239], v[102:105]
	v_mfma_f32_16x16x32_bf16 v[98:101], v[192:195], v[236:239], v[98:101]
	v_mfma_f32_16x16x32_bf16 v[126:129], v[188:191], v[224:227], v[126:129]
	v_mfma_f32_16x16x32_bf16 v[122:125], v[196:199], v[224:227], v[122:125]
	v_mfma_f32_16x16x32_bf16 v[118:121], v[188:191], v[228:231], v[118:121]
	v_mfma_f32_16x16x32_bf16 v[114:117], v[196:199], v[228:231], v[114:117]
	v_mfma_f32_16x16x32_bf16 v[110:113], v[188:191], v[240:243], v[110:113]
	v_mfma_f32_16x16x32_bf16 v[106:109], v[196:199], v[240:243], v[106:109]
	v_mfma_f32_16x16x32_bf16 v[102:105], v[188:191], v[244:247], v[102:105]
	v_mfma_f32_16x16x32_bf16 v[98:101], v[196:199], v[244:247], v[98:101]
	s_setprio 0
	s_setprio 1
	v_mfma_f32_16x16x32_bf16 v[62:65], v[200:203], v[216:219], v[62:65]
	v_mfma_f32_16x16x32_bf16 v[58:61], v[208:211], v[216:219], v[58:61]
	v_mfma_f32_16x16x32_bf16 v[54:57], v[200:203], v[220:223], v[54:57]
	v_mfma_f32_16x16x32_bf16 v[50:53], v[208:211], v[220:223], v[50:53]
	v_mfma_f32_16x16x32_bf16 v[46:49], v[200:203], v[232:235], v[46:49]
	v_mfma_f32_16x16x32_bf16 v[42:45], v[208:211], v[232:235], v[42:45]
	v_mfma_f32_16x16x32_bf16 v[38:41], v[200:203], v[236:239], v[38:41]
	v_mfma_f32_16x16x32_bf16 v[34:37], v[208:211], v[236:239], v[34:37]
	v_mfma_f32_16x16x32_bf16 v[62:65], v[204:207], v[224:227], v[62:65]
	v_mfma_f32_16x16x32_bf16 v[58:61], v[212:215], v[224:227], v[58:61]
	v_mfma_f32_16x16x32_bf16 v[54:57], v[204:207], v[228:231], v[54:57]
	v_mfma_f32_16x16x32_bf16 v[50:53], v[212:215], v[228:231], v[50:53]
	v_mfma_f32_16x16x32_bf16 v[46:49], v[204:207], v[240:243], v[46:49]
	v_mfma_f32_16x16x32_bf16 v[42:45], v[212:215], v[240:243], v[42:45]
	v_mfma_f32_16x16x32_bf16 v[38:41], v[204:207], v[244:247], v[38:41]
	v_mfma_f32_16x16x32_bf16 v[34:37], v[212:215], v[244:247], v[34:37]
	s_setprio 0
	s_barrier
	s_add_i32 s73, s87, s76
	s_mov_b32 m0, s73
	ds_read_b128 v[216:219], v178 offset:16384
	ds_read_b128 v[220:223], v178 offset:18432
	ds_read_b128 v[224:227], v179 offset:16384
	ds_read_b128 v[228:231], v179 offset:18432
	ds_read_b128 v[232:235], v178 offset:20480
	ds_read_b128 v[236:239], v178 offset:22528
	ds_read_b128 v[240:243], v179 offset:20480
	ds_read_b128 v[244:247], v179 offset:22528
	global_load_lds_dwordx4 v142, s[68:69]
	s_add_i32 m0, s73, 0x2000
	s_add_u32 vcc_lo, s68, 0x80000
	s_addc_u32 vcc_hi, s69, 0
	s_add_i32 s73, s89, s76
	global_load_lds_dwordx4 v144, s[68:69]
	s_mov_b32 m0, s73
	s_nop 0
	global_load_lds_dwordx4 v142, vcc
	s_add_i32 m0, s73, 0x2000
	s_nop 0
	global_load_lds_dwordx4 v144, vcc
	s_waitcnt vmcnt(6)
	s_waitcnt lgkmcnt(0)
	s_barrier
	s_setprio 1
	s_waitcnt lgkmcnt(0)
	v_mfma_f32_16x16x32_bf16 v[94:97], v[184:187], v[216:219], v[94:97]
	v_mfma_f32_16x16x32_bf16 v[90:93], v[192:195], v[216:219], v[90:93]
	v_mfma_f32_16x16x32_bf16 v[86:89], v[184:187], v[220:223], v[86:89]
	v_mfma_f32_16x16x32_bf16 v[82:85], v[192:195], v[220:223], v[82:85]
	v_mfma_f32_16x16x32_bf16 v[78:81], v[184:187], v[232:235], v[78:81]
	v_mfma_f32_16x16x32_bf16 v[74:77], v[192:195], v[232:235], v[74:77]
	v_mfma_f32_16x16x32_bf16 v[70:73], v[184:187], v[236:239], v[70:73]
	v_mfma_f32_16x16x32_bf16 v[66:69], v[192:195], v[236:239], v[66:69]
	v_mfma_f32_16x16x32_bf16 v[94:97], v[188:191], v[224:227], v[94:97]
	v_mfma_f32_16x16x32_bf16 v[90:93], v[196:199], v[224:227], v[90:93]
	v_mfma_f32_16x16x32_bf16 v[86:89], v[188:191], v[228:231], v[86:89]
	v_mfma_f32_16x16x32_bf16 v[82:85], v[196:199], v[228:231], v[82:85]
	v_mfma_f32_16x16x32_bf16 v[78:81], v[188:191], v[240:243], v[78:81]
	v_mfma_f32_16x16x32_bf16 v[74:77], v[196:199], v[240:243], v[74:77]
	v_mfma_f32_16x16x32_bf16 v[70:73], v[188:191], v[244:247], v[70:73]
	v_mfma_f32_16x16x32_bf16 v[66:69], v[196:199], v[244:247], v[66:69]
	s_setprio 0
	s_setprio 1
	v_mfma_f32_16x16x32_bf16 v[30:33], v[200:203], v[216:219], v[30:33]
	v_mfma_f32_16x16x32_bf16 v[26:29], v[208:211], v[216:219], v[26:29]
	v_mfma_f32_16x16x32_bf16 v[22:25], v[200:203], v[220:223], v[22:25]
	v_mfma_f32_16x16x32_bf16 v[18:21], v[208:211], v[220:223], v[18:21]
	v_mfma_f32_16x16x32_bf16 v[14:17], v[200:203], v[232:235], v[14:17]
	v_mfma_f32_16x16x32_bf16 v[10:13], v[208:211], v[232:235], v[10:13]
	v_mfma_f32_16x16x32_bf16 v[6:9], v[200:203], v[236:239], v[6:9]
	v_mfma_f32_16x16x32_bf16 v[2:5], v[208:211], v[236:239], v[2:5]
	v_mfma_f32_16x16x32_bf16 v[30:33], v[204:207], v[224:227], v[30:33]
	v_mfma_f32_16x16x32_bf16 v[26:29], v[212:215], v[224:227], v[26:29]
	v_mfma_f32_16x16x32_bf16 v[22:25], v[204:207], v[228:231], v[22:25]
	v_mfma_f32_16x16x32_bf16 v[18:21], v[212:215], v[228:231], v[18:21]
	v_mfma_f32_16x16x32_bf16 v[14:17], v[204:207], v[240:243], v[14:17]
	v_mfma_f32_16x16x32_bf16 v[10:13], v[212:215], v[240:243], v[10:13]
	v_mfma_f32_16x16x32_bf16 v[6:9], v[204:207], v[244:247], v[6:9]
	v_mfma_f32_16x16x32_bf16 v[2:5], v[212:215], v[244:247], v[2:5]
	s_setprio 0
	s_barrier
.Lp1_blk3:
	ds_read_b128 v[184:187], v175 offset:32768
	ds_read_b128 v[188:191], v176 offset:32768
	ds_read_b128 v[192:195], v175 offset:34816
	ds_read_b128 v[196:199], v176 offset:34816
	ds_read_b128 v[200:203], v175 offset:49152
	ds_read_b128 v[204:207], v176 offset:49152
	ds_read_b128 v[208:211], v175 offset:51200
	ds_read_b128 v[212:215], v176 offset:51200
	s_mov_b32 m0, s77
	ds_read_b128 v[216:219], v178 offset:32768
	ds_read_b128 v[220:223], v178 offset:34816
	ds_read_b128 v[224:227], v179 offset:32768
	ds_read_b128 v[228:231], v179 offset:34816
	ds_read_b128 v[232:235], v178 offset:36864
	ds_read_b128 v[236:239], v178 offset:38912
	ds_read_b128 v[240:243], v179 offset:36864
	ds_read_b128 v[244:247], v179 offset:38912
	global_load_lds_dwordx4 v166, s[70:71]
	s_mov_b32 m0, s78
	s_nop 0
	global_load_lds_dwordx4 v164, s[70:71]
	s_mov_b32 m0, s79
	s_nop 0
	global_load_lds_dwordx4 v162, s[70:71]
	s_mov_b32 m0, s80
	s_nop 0
	global_load_lds_dwordx4 v160, s[70:71]
	s_waitcnt vmcnt(8)
	s_waitcnt lgkmcnt(0)
	s_barrier
	s_setprio 1
	s_waitcnt lgkmcnt(0)
	v_mfma_f32_16x16x32_bf16 v[126:129], v[184:187], v[216:219], v[126:129]
	v_mfma_f32_16x16x32_bf16 v[122:125], v[192:195], v[216:219], v[122:125]
	v_mfma_f32_16x16x32_bf16 v[118:121], v[184:187], v[220:223], v[118:121]
	v_mfma_f32_16x16x32_bf16 v[114:117], v[192:195], v[220:223], v[114:117]
	v_mfma_f32_16x16x32_bf16 v[110:113], v[184:187], v[232:235], v[110:113]
	v_mfma_f32_16x16x32_bf16 v[106:109], v[192:195], v[232:235], v[106:109]
	v_mfma_f32_16x16x32_bf16 v[102:105], v[184:187], v[236:239], v[102:105]
	v_mfma_f32_16x16x32_bf16 v[98:101], v[192:195], v[236:239], v[98:101]
	v_mfma_f32_16x16x32_bf16 v[126:129], v[188:191], v[224:227], v[126:129]
	v_mfma_f32_16x16x32_bf16 v[122:125], v[196:199], v[224:227], v[122:125]
	v_mfma_f32_16x16x32_bf16 v[118:121], v[188:191], v[228:231], v[118:121]
	v_mfma_f32_16x16x32_bf16 v[114:117], v[196:199], v[228:231], v[114:117]
	v_mfma_f32_16x16x32_bf16 v[110:113], v[188:191], v[240:243], v[110:113]
	v_mfma_f32_16x16x32_bf16 v[106:109], v[196:199], v[240:243], v[106:109]
	v_mfma_f32_16x16x32_bf16 v[102:105], v[188:191], v[244:247], v[102:105]
	v_mfma_f32_16x16x32_bf16 v[98:101], v[196:199], v[244:247], v[98:101]
	s_setprio 0
	s_setprio 1
	v_mfma_f32_16x16x32_bf16 v[62:65], v[200:203], v[216:219], v[62:65]
	v_mfma_f32_16x16x32_bf16 v[58:61], v[208:211], v[216:219], v[58:61]
	v_mfma_f32_16x16x32_bf16 v[54:57], v[200:203], v[220:223], v[54:57]
	v_mfma_f32_16x16x32_bf16 v[50:53], v[208:211], v[220:223], v[50:53]
	v_mfma_f32_16x16x32_bf16 v[46:49], v[200:203], v[232:235], v[46:49]
	v_mfma_f32_16x16x32_bf16 v[42:45], v[208:211], v[232:235], v[42:45]
	v_mfma_f32_16x16x32_bf16 v[38:41], v[200:203], v[236:239], v[38:41]
	v_mfma_f32_16x16x32_bf16 v[34:37], v[208:211], v[236:239], v[34:37]
	v_mfma_f32_16x16x32_bf16 v[62:65], v[204:207], v[224:227], v[62:65]
	v_mfma_f32_16x16x32_bf16 v[58:61], v[212:215], v[224:227], v[58:61]
	v_mfma_f32_16x16x32_bf16 v[54:57], v[204:207], v[228:231], v[54:57]
	v_mfma_f32_16x16x32_bf16 v[50:53], v[212:215], v[228:231], v[50:53]
	v_mfma_f32_16x16x32_bf16 v[46:49], v[204:207], v[240:243], v[46:49]
	v_mfma_f32_16x16x32_bf16 v[42:45], v[212:215], v[240:243], v[42:45]
	v_mfma_f32_16x16x32_bf16 v[38:41], v[204:207], v[244:247], v[38:41]
	v_mfma_f32_16x16x32_bf16 v[34:37], v[212:215], v[244:247], v[34:37]
	s_setprio 0
	s_barrier
	s_add_i32 s70, s92, s76
	s_add_u32 vcc_lo, s68, s8
	s_addc_u32 vcc_hi, s69, s9
	s_mov_b32 m0, s70
	ds_read_b128 v[160:163], v178 offset:49152
	ds_read_b128 v[164:167], v178 offset:51200
	ds_read_b128 v[216:219], v179 offset:49152
	ds_read_b128 v[220:223], v179 offset:51200
	ds_read_b128 v[224:227], v178 offset:53248
	ds_read_b128 v[228:231], v178 offset:55296
	ds_read_b128 v[232:235], v179 offset:53248
	ds_read_b128 v[236:239], v179 offset:55296
	global_load_lds_dwordx4 v142, vcc
	s_add_i32 m0, s70, 0x2000
	s_add_u32 s68, s68, 0x80080
	s_addc_u32 s69, s69, 0
	s_add_i32 s70, s94, s76
	global_load_lds_dwordx4 v144, vcc
	s_mov_b32 m0, s70
	s_nop 0
	global_load_lds_dwordx4 v142, s[68:69]
	s_add_i32 m0, s70, 0x2000
	s_nop 0
	global_load_lds_dwordx4 v144, s[68:69]
	s_waitcnt vmcnt(6)
	s_waitcnt lgkmcnt(0)
	s_barrier
	s_setprio 1
	s_waitcnt lgkmcnt(0)
	v_mfma_f32_16x16x32_bf16 v[94:97], v[184:187], v[160:163], v[94:97]
	v_mfma_f32_16x16x32_bf16 v[90:93], v[192:195], v[160:163], v[90:93]
	v_mfma_f32_16x16x32_bf16 v[86:89], v[184:187], v[164:167], v[86:89]
	v_mfma_f32_16x16x32_bf16 v[82:85], v[192:195], v[164:167], v[82:85]
	v_mfma_f32_16x16x32_bf16 v[78:81], v[184:187], v[224:227], v[78:81]
	v_mfma_f32_16x16x32_bf16 v[74:77], v[192:195], v[224:227], v[74:77]
	v_mfma_f32_16x16x32_bf16 v[70:73], v[184:187], v[228:231], v[70:73]
	v_mfma_f32_16x16x32_bf16 v[66:69], v[192:195], v[228:231], v[66:69]
	v_mfma_f32_16x16x32_bf16 v[94:97], v[188:191], v[216:219], v[94:97]
	v_mfma_f32_16x16x32_bf16 v[90:93], v[196:199], v[216:219], v[90:93]
	v_mfma_f32_16x16x32_bf16 v[86:89], v[188:191], v[220:223], v[86:89]
	v_mfma_f32_16x16x32_bf16 v[82:85], v[196:199], v[220:223], v[82:85]
	v_mfma_f32_16x16x32_bf16 v[78:81], v[188:191], v[232:235], v[78:81]
	v_mfma_f32_16x16x32_bf16 v[74:77], v[196:199], v[232:235], v[74:77]
	v_mfma_f32_16x16x32_bf16 v[70:73], v[188:191], v[236:239], v[70:73]
	v_mfma_f32_16x16x32_bf16 v[66:69], v[196:199], v[236:239], v[66:69]
	s_setprio 0
	s_setprio 1
	v_mfma_f32_16x16x32_bf16 v[30:33], v[200:203], v[160:163], v[30:33]
	v_mfma_f32_16x16x32_bf16 v[26:29], v[208:211], v[160:163], v[26:29]
	v_mfma_f32_16x16x32_bf16 v[22:25], v[200:203], v[164:167], v[22:25]
	v_mfma_f32_16x16x32_bf16 v[18:21], v[208:211], v[164:167], v[18:21]
	v_mfma_f32_16x16x32_bf16 v[14:17], v[200:203], v[224:227], v[14:17]
	v_mfma_f32_16x16x32_bf16 v[10:13], v[208:211], v[224:227], v[10:13]
	v_mfma_f32_16x16x32_bf16 v[6:9], v[200:203], v[228:231], v[6:9]
	v_mfma_f32_16x16x32_bf16 v[2:5], v[208:211], v[228:231], v[2:5]
	v_mfma_f32_16x16x32_bf16 v[30:33], v[204:207], v[216:219], v[30:33]
	v_mfma_f32_16x16x32_bf16 v[26:29], v[212:215], v[216:219], v[26:29]
	v_mfma_f32_16x16x32_bf16 v[22:25], v[204:207], v[220:223], v[22:25]
	v_mfma_f32_16x16x32_bf16 v[18:21], v[212:215], v[220:223], v[18:21]
	v_mfma_f32_16x16x32_bf16 v[14:17], v[204:207], v[232:235], v[14:17]
	v_mfma_f32_16x16x32_bf16 v[10:13], v[212:215], v[232:235], v[10:13]
	v_mfma_f32_16x16x32_bf16 v[6:9], v[204:207], v[236:239], v[6:9]
	v_mfma_f32_16x16x32_bf16 v[2:5], v[212:215], v[236:239], v[2:5]
	s_setprio 0
	s_barrier
	s_add_i32 s72, s72, 2
	s_add_u32 s66, s66, 0x100
	s_addc_u32 s67, s67, 0
	s_cmp_gt_u32 s72, 29
	s_cbranch_scc1 .LBB0_105
